# c1_coop
# speedup vs baseline: 1.0075x; 1.0075x over previous
.LBB3_3:
	v_lshrrev_b32_e32 v2, 2, v0
	v_sub_u32_e32 v2, 0, v2
	s_lshr_b32 s9, s5, 2
	s_load_dwordx2 s[2:3], s[0:1], 0x30
	s_load_dwordx2 s[14:15], s[0:1], 0x8
	v_and_b32_e32 v34, 15, v0
	v_bitop3_b32 v2, v1, v2, 3 bitop3:0x78
	s_and_b32 s9, s9, 64
	s_lshl_b32 s10, s6, 5
	v_lshlrev_b32_e32 v35, 4, v2
	v_or_b32_e32 v2, s9, v34
	s_and_b32 s10, s10, 0x60
	v_lshlrev_b32_e32 v36, 6, v2
	v_or_b32_e32 v2, s10, v34
	v_lshlrev_b32_e32 v37, 6, v2
	v_mov_b32_e32 v2, 0
	s_mov_b32 s8, 0
	s_mov_b32 s11, 32
	v_mov_b32_e32 v3, v2
	v_mov_b32_e32 v4, v2
	v_mov_b32_e32 v5, v2
	v_mov_b32_e32 v10, v2
	v_mov_b32_e32 v11, v2
	v_mov_b32_e32 v12, v2
	v_mov_b32_e32 v13, v2
	v_mov_b32_e32 v6, v2
	v_mov_b32_e32 v7, v2
	v_mov_b32_e32 v8, v2
	v_mov_b32_e32 v9, v2
	v_mov_b32_e32 v18, v2
	v_mov_b32_e32 v19, v2
	v_mov_b32_e32 v20, v2
	v_mov_b32_e32 v21, v2
	v_mov_b32_e32 v14, v2
	v_mov_b32_e32 v15, v2
	v_mov_b32_e32 v16, v2
	v_mov_b32_e32 v17, v2
	v_mov_b32_e32 v26, v2
	v_mov_b32_e32 v27, v2
	v_mov_b32_e32 v28, v2
	v_mov_b32_e32 v29, v2
	v_mov_b32_e32 v22, v2
	v_mov_b32_e32 v23, v2
	v_mov_b32_e32 v24, v2
	v_mov_b32_e32 v25, v2
	v_mov_b32_e32 v30, v2
	v_mov_b32_e32 v31, v2
	v_mov_b32_e32 v32, v2
	v_mov_b32_e32 v33, v2
	v_and_b32_e32 v62, 63, v0
	v_lshrrev_b32_e32 v63, 2, v62
	v_and_b32_e32 v62, 3, v62
	v_sub_u32_e32 v64, 0, v1
	v_and_b32_e32 v64, 3, v64
	v_xor_b32_e32 v62, v62, v64
	v_lshlrev_b32_e32 v62, 4, v62
	v_lshl_or_b32 v62, v63, 11, v62
	s_lshl_b32 s13, s6, 4
	s_add_i32 s13, s13, s4
	s_lshl_b32 s13, s13, 11
	s_lshl_b32 s16, s6, 10
	s_add_i32 s16, s16, 0x2000
	s_waitcnt lgkmcnt(0)
	s_add_u32 s14, s14, s13
	s_addc_u32 s15, s15, 0
	s_add_i32 m0, s16, 0
	s_nop 0
	global_load_lds_dwordx4 v62, s[14:15] offset:0
	s_add_i32 m0, s16, 16320
	s_nop 0
	global_load_lds_dwordx4 v62, s[14:15] offset:64
	s_add_i32 m0, s16, 32640
	s_nop 0
	global_load_lds_dwordx4 v62, s[14:15] offset:128
	s_add_i32 m0, s16, 48960
	s_nop 0
	global_load_lds_dwordx4 v62, s[14:15] offset:192
	v_add_u32_e32 v62, 0x100, v62
	s_mov_b32 s17, 4
.Lg1_cloop:
	s_lshl_b32 s12, s8, 14
	v_add3_u32 v42, s12, v37, v35
	v_add3_u32 v58, s12, v36, v35
	s_waitcnt vmcnt(3)
	s_barrier
	ds_read_b128 v[38:41], v42 offset:8192
	ds_read_b128 v[42:45], v42 offset:9216
	ds_read_b128 v[46:49], v58
	ds_read_b128 v[50:53], v58 offset:1024
	ds_read_b128 v[54:57], v58 offset:2048
	ds_read_b128 v[58:61], v58 offset:3072
	s_lshl_b32 s13, s17, 14
	s_add_i32 m0, s13, s16
	s_add_i32 s13, s17, 1
	global_load_lds_dwordx4 v62, s[14:15]
	s_cmp_lg_u32 s17, 4
	s_cselect_b32 s17, s13, 0
	v_add_u32_e32 v62, 64, v62
	s_waitcnt lgkmcnt(0)
	v_mfma_f32_16x16x32_f16 v[30:33], v[46:49], v[38:41], v[30:33]
	s_add_i32 s12, s8, 1
	s_cmp_lg_u32 s8, 4
	s_cselect_b32 s8, s12, 0
	v_mfma_f32_16x16x32_f16 v[22:25], v[46:49], v[42:45], v[22:25]
	s_add_i32 s11, s11, -1
	s_cmp_eq_u32 s11, 0
	v_mfma_f32_16x16x32_f16 v[26:29], v[50:53], v[38:41], v[26:29]
	v_mfma_f32_16x16x32_f16 v[14:17], v[50:53], v[42:45], v[14:17]
	v_mfma_f32_16x16x32_f16 v[18:21], v[54:57], v[38:41], v[18:21]
	v_mfma_f32_16x16x32_f16 v[6:9], v[54:57], v[42:45], v[6:9]
	v_mfma_f32_16x16x32_f16 v[10:13], v[58:61], v[38:41], v[10:13]
	v_mfma_f32_16x16x32_f16 v[2:5], v[58:61], v[42:45], v[2:5]
	s_cbranch_scc0 .Lg1_cloop
	s_or_b32 s8, s10, s4
	v_or_b32_e32 v35, s8, v34
	v_lshl_or_b32 v34, v1, 2, s9
	v_mov_b32_e32 v37, 0
	v_or_b32_e32 v34, s7, v34
	v_lshlrev_b32_e32 v36, 12, v35
	v_mov_b32_e32 v35, v37
	v_lshl_add_u64 v[38:39], s[2:3], 0, v[36:37]
	v_lshlrev_b64 v[40:41], 2, v[34:35]
	v_lshl_add_u64 v[42:43], v[38:39], 0, v[40:41]
	s_mov_b64 s[2:3], 0x10000
	v_lshl_add_u64 v[44:45], v[42:43], 0, s[2:3]
	global_store_dwordx4 v[42:43], v[30:33], off sc1
	global_store_dwordx4 v[42:43], v[26:29], off offset:64 sc1
	global_store_dwordx4 v[42:43], v[18:21], off offset:128 sc1
	global_store_dwordx4 v[42:43], v[10:13], off offset:192 sc1
	global_store_dwordx4 v[44:45], v[22:25], off sc1
	global_store_dwordx4 v[44:45], v[14:17], off offset:64 sc1
	global_store_dwordx4 v[44:45], v[6:9], off offset:128 sc1
	global_store_dwordx4 v[44:45], v[2:5], off offset:192 sc1
	s_branch .LBB3_2
.LBB3_6:
	s_load_dwordx4 s[0:3], s[0:1], 0x0
	s_add_i32 s9, s6, -8
	s_mov_b32 s28, s7
	s_mov_b32 s29, s4
	v_and_b32_e32 v1, 63, v0
	v_bfe_u32 v3, v0, 4, 2
	v_lshrrev_b32_e32 v2, 2, v1
	v_sub_u32_e32 v3, 0, v3
	v_and_b32_e32 v3, 3, v3
	v_and_b32_e32 v4, 3, v1
	v_xor_b32_e32 v3, v3, v4
	v_lshlrev_b32_e32 v3, 4, v3
	v_lshl_or_b32 v2, v2, 11, v3
	s_lshl_b32 s4, s9, 4
	s_add_i32 s5, s28, s4
	s_lshl_b32 s5, s5, 11
	s_add_i32 s6, s29, s4
	s_lshl_b32 s6, s6, 11
	s_lshl_b32 s8, s9, 10
	s_waitcnt lgkmcnt(0)
	s_add_u32 s10, s0, s5
	s_addc_u32 s11, s1, 0
	s_add_u32 s12, s10, 131072
	s_addc_u32 s13, s11, 0
	v_mov_b32_e32 v5, v2
	v_mov_b32_e32 v6, v2
	s_add_i32 m0, s8, 0
	s_nop 0
	global_load_lds_dwordx4 v5, s[10:11]
	s_add_i32 m0, s8, 4096
	s_nop 0
	global_load_lds_dwordx4 v5, s[12:13]
	v_add_u32_e32 v5, 64, v5
	v_add_u32_e32 v6, 64, v6
	s_add_i32 m0, s8, 16384
	s_nop 0
	global_load_lds_dwordx4 v5, s[10:11]
	s_add_i32 m0, s8, 20480
	s_nop 0
	global_load_lds_dwordx4 v5, s[12:13]
	v_add_u32_e32 v5, 64, v5
	v_add_u32_e32 v6, 64, v6
	s_add_i32 m0, s8, 32768
	s_nop 0
	global_load_lds_dwordx4 v5, s[10:11]
	s_add_i32 m0, s8, 36864
	s_nop 0
	global_load_lds_dwordx4 v5, s[12:13]
	v_add_u32_e32 v5, 64, v5
	v_add_u32_e32 v6, 64, v6
	s_add_i32 m0, s8, 49152
	s_nop 0
	global_load_lds_dwordx4 v5, s[10:11]
	s_add_i32 m0, s8, 53248
	s_nop 0
	global_load_lds_dwordx4 v5, s[12:13]
	v_add_u32_e32 v5, 64, v5
	v_add_u32_e32 v6, 64, v6
	s_mov_b32 s29, 4
	s_mov_b32 s30, 28
.Lg1_ploop:
	s_mul_i32 s28, s29, 16384
	s_add_i32 s28, s28, s8
	s_waitcnt vmcnt(6)
	s_barrier
	s_mov_b32 m0, s28
	s_add_i32 s28, s28, 0x1000
	global_load_lds_dwordx4 v5, s[10:11]
	s_mov_b32 m0, s28
	s_add_i32 s28, s28, 0x1000
	global_load_lds_dwordx4 v5, s[12:13]
	v_add_u32_e32 v5, 64, v5
	v_add_u32_e32 v6, 64, v6
	s_add_i32 s31, s29, 1
	s_cmp_lg_u32 s29, 4
	s_cselect_b32 s29, s31, 0
	s_add_i32 s30, s30, -1
	s_cmp_eq_u32 s30, 0
	s_cbranch_scc0 .Lg1_ploop
	s_waitcnt vmcnt(6)
	s_barrier
	s_waitcnt vmcnt(4)
	s_barrier
	s_waitcnt vmcnt(2)
	s_barrier
	s_waitcnt vmcnt(0)
	s_barrier
	s_endpgm

	.amdhsa_kernel _Z11gemm_kernelILi1ELi4ELi2ELi5EEvPKDF16_S1_PK15HIP_vector_typeIfLj4EEPDF16_S6_S6_Pf
		.amdhsa_group_segment_fixed_size 0
		.amdhsa_private_segment_fixed_size 0
		.amdhsa_kernarg_size 56
		.amdhsa_user_sgpr_count 2
		.amdhsa_user_sgpr_dispatch_ptr 0
		.amdhsa_user_sgpr_queue_ptr 0
		.amdhsa_user_sgpr_kernarg_segment_ptr 1
		.amdhsa_user_sgpr_dispatch_id 0
		.amdhsa_user_sgpr_kernarg_preload_length 0
		.amdhsa_user_sgpr_kernarg_preload_offset 0
		.amdhsa_user_sgpr_private_segment_size 0
		.amdhsa_uses_dynamic_stack 0
		.amdhsa_enable_private_segment 0
		.amdhsa_system_sgpr_workgroup_id_x 1
		.amdhsa_system_sgpr_workgroup_id_y 0
		.amdhsa_system_sgpr_workgroup_id_z 0
		.amdhsa_system_sgpr_workgroup_info 0
		.amdhsa_system_vgpr_workitem_id 0
		.amdhsa_next_free_vgpr 66
		.amdhsa_next_free_sgpr 32
		.amdhsa_accum_offset 68
		.amdhsa_reserve_vcc 1
		.amdhsa_float_round_mode_32 0
		.amdhsa_float_round_mode_16_64 0
		.amdhsa_float_denorm_mode_32 3
		.amdhsa_float_denorm_mode_16_64 3
		.amdhsa_dx10_clamp 1
		.amdhsa_ieee_mode 1
		.amdhsa_fp16_overflow 0
		.amdhsa_tg_split 0
		.amdhsa_exception_fp_ieee_invalid_op 0
		.amdhsa_exception_fp_denorm_src 0
		.amdhsa_exception_fp_ieee_div_zero 0
		.amdhsa_exception_fp_ieee_overflow 0
		.amdhsa_exception_fp_ieee_underflow 0
		.amdhsa_exception_fp_ieee_inexact 0
		.amdhsa_exception_int_div_zero 0
	.end_amdhsa_kernel

amdhsa.kernels:
  - .agpr_count:     0
    .args:
      - .address_space:  global
        .offset:         0
        .size:           8
        .value_kind:     global_buffer
      - .address_space:  global
        .offset:         8
        .size:           8
        .value_kind:     global_buffer
      - .address_space:  global
        .offset:         16
        .size:           8
        .value_kind:     global_buffer
      - .address_space:  global
        .offset:         24
        .size:           8
        .value_kind:     global_buffer
      - .address_space:  global
        .offset:         32
        .size:           8
        .value_kind:     global_buffer
      - .actual_access:  write_only
        .address_space:  global
        .offset:         40
        .size:           8
        .value_kind:     global_buffer
      - .actual_access:  write_only
        .address_space:  global
        .offset:         48
        .size:           8
        .value_kind:     global_buffer
      - .actual_access:  write_only
        .address_space:  global
        .offset:         56
        .size:           8
        .value_kind:     global_buffer
      - .actual_access:  write_only
        .address_space:  global
        .offset:         64
        .size:           8
        .value_kind:     global_buffer
    .group_segment_fixed_size: 0
    .kernarg_segment_align: 8
    .kernarg_segment_size: 72
    .language:       OpenCL C
    .language_version:
      - 2
      - 0
    .max_flat_workgroup_size: 256
    .name:           _Z11prep_kernelPKfS0_S0_S0_S0_PDF16_S1_S1_P15HIP_vector_typeIfLj2EE
    .private_segment_fixed_size: 0
    .sgpr_count:     38
    .sgpr_spill_count: 0
    .symbol:         _Z11prep_kernelPKfS0_S0_S0_S0_PDF16_S1_S1_P15HIP_vector_typeIfLj2EE.kd
    .uniform_work_group_size: 1
    .uses_dynamic_stack: false
    .vgpr_count:     44
    .vgpr_spill_count: 0
    .wavefront_size: 64
  - .agpr_count:     0
    .args:
      - .address_space:  global
        .offset:         0
        .size:           8
        .value_kind:     global_buffer
      - .address_space:  global
        .offset:         8
        .size:           8
        .value_kind:     global_buffer
      - .address_space:  global
        .offset:         16
        .size:           8
        .value_kind:     global_buffer
      - .address_space:  global
        .offset:         24
        .size:           8
        .value_kind:     global_buffer
    .group_segment_fixed_size: 0
    .kernarg_segment_align: 8
    .kernarg_segment_size: 32
    .language:       OpenCL C
    .language_version:
      - 2
      - 0
    .max_flat_workgroup_size: 256
    .name:           _Z10attn64_fwdPKDF16_S0_S0_PDF16_
    .private_segment_fixed_size: 0
    .sgpr_count:     55
    .sgpr_spill_count: 0
    .symbol:         _Z10attn64_fwdPKDF16_S0_S0_PDF16_.kd
    .uniform_work_group_size: 1
    .uses_dynamic_stack: false
    .vgpr_count:     248
    .vgpr_spill_count: 0
    .wavefront_size: 64
  - .agpr_count:     0
    .args:
      - .address_space:  global
        .offset:         0
        .size:           8
        .value_kind:     global_buffer
      - .address_space:  global
        .offset:         8
        .size:           8
        .value_kind:     global_buffer
      - .actual_access:  read_only
        .address_space:  global
        .offset:         16
        .size:           8
        .value_kind:     global_buffer
      - .actual_access:  write_only
        .address_space:  global
        .offset:         24
        .size:           8
        .value_kind:     global_buffer
      - .actual_access:  write_only
        .address_space:  global
        .offset:         32
        .size:           8
        .value_kind:     global_buffer
      - .actual_access:  write_only
        .address_space:  global
        .offset:         40
        .size:           8
        .value_kind:     global_buffer
      - .actual_access:  read_only
        .address_space:  global
        .offset:         48
        .size:           8
        .value_kind:     global_buffer
    .group_segment_fixed_size: 0
    .kernarg_segment_align: 8
    .kernarg_segment_size: 56
    .language:       OpenCL C
    .language_version:
      - 2
      - 0
    .max_flat_workgroup_size: 768
    .name:           _Z11gemm_kernelILi0ELi6ELi4ELi5EEvPKDF16_S1_PK15HIP_vector_typeIfLj4EEPDF16_S6_S6_Pf
    .private_segment_fixed_size: 0
    .sgpr_count:     56
    .sgpr_spill_count: 0
    .symbol:         _Z11gemm_kernelILi0ELi6ELi4ELi5EEvPKDF16_S1_PK15HIP_vector_typeIfLj4EEPDF16_S6_S6_Pf.kd
    .uniform_work_group_size: 1
    .uses_dynamic_stack: false
    .vgpr_count:     168
    .vgpr_spill_count: 0
    .wavefront_size: 64
  - .agpr_count:     0
    .args:
      - .address_space:  global
        .offset:         0
        .size:           8
        .value_kind:     global_buffer
      - .address_space:  global
        .offset:         8
        .size:           8
        .value_kind:     global_buffer
      - .actual_access:  read_only
        .address_space:  global
        .offset:         16
        .size:           8
        .value_kind:     global_buffer
      - .actual_access:  read_only
        .address_space:  global
        .offset:         24
        .size:           8
        .value_kind:     global_buffer
      - .actual_access:  read_only
        .address_space:  global
        .offset:         32
        .size:           8
        .value_kind:     global_buffer
      - .actual_access:  read_only
        .address_space:  global
        .offset:         40
        .size:           8
        .value_kind:     global_buffer
      - .actual_access:  write_only
        .address_space:  global
        .offset:         48
        .size:           8
        .value_kind:     global_buffer
    .group_segment_fixed_size: 0
    .kernarg_segment_align: 8
    .kernarg_segment_size: 56
    .language:       OpenCL C
    .language_version:
      - 2
      - 0
    .max_flat_workgroup_size: 768
    .name:           _Z11gemm_kernelILi1ELi4ELi2ELi5EEvPKDF16_S1_PK15HIP_vector_typeIfLj4EEPDF16_S6_S6_Pf
    .private_segment_fixed_size: 0
    .sgpr_count:     38
    .sgpr_spill_count: 0
    .symbol:         _Z11gemm_kernelILi1ELi4ELi2ELi5EEvPKDF16_S1_PK15HIP_vector_typeIfLj4EEPDF16_S6_S6_Pf.kd
    .uniform_work_group_size: 1
    .uses_dynamic_stack: false
    .vgpr_count:     66
    .vgpr_spill_count: 0
    .wavefront_size: 64
